# speedup vs baseline: 1.0153x; 1.0089x over previous
.LBB1_4:
	s_load_dwordx2 s[0:1], s[0:1], 0x0
	v_add_u32_e32 v2, 0xffffff00, v0
	v_ashrrev_i32_e32 v20, 4, v2
	v_add_u32_e32 v2, s12, v20
	v_ashrrev_i32_e32 v3, 31, v2
	v_lshlrev_b64 v[2:3], 12, v[2:3]
	s_lshl_b32 s2, s3, 6
	s_waitcnt lgkmcnt(0)
	v_lshl_add_u64 v[2:3], s[0:1], 0, v[2:3]
	v_lshlrev_b32_e32 v4, 4, v1
	v_mov_b32_e32 v5, 0
	s_and_b32 s6, s2, 0x3c0
	s_mov_b32 s1, 0
	v_lshl_add_u64 v[2:3], v[2:3], 0, v[4:5]
	s_lshl_b32 s0, s6, 2
	v_lshl_add_u64 v[16:17], v[2:3], 0, s[0:1]
	s_mov_b32 s3, 0x10000
	v_add_co_u32_e32 v12, vcc, s3, v16
	s_mov_b32 s4, 0x20000
	s_nop 0
	v_addc_co_u32_e32 v13, vcc, 0, v17, vcc
	global_load_dwordx4 v[4:7], v[16:17], off sc0 sc1 nt
	global_load_dwordx4 v[8:11], v[12:13], off sc0 sc1 nt
	v_add_co_u32_e32 v12, vcc, s4, v16
	s_mov_b32 s5, 0x30000
	s_nop 0
	v_addc_co_u32_e32 v13, vcc, 0, v17, vcc
	s_add_i32 s0, s2, 64
	global_load_dwordx4 v[12:15], v[12:13], off sc0 sc1 nt
	v_add_co_u32_e32 v16, vcc, s5, v16
	s_and_b32 s0, s0, 0x3c0
	s_nop 0
	v_addc_co_u32_e32 v17, vcc, 0, v17, vcc
	s_lshl_b32 s0, s0, 2
	global_load_dwordx4 v[16:19], v[16:17], off sc0 sc1 nt
	v_lshl_add_u64 v[28:29], v[2:3], 0, s[0:1]
	v_lshrrev_b32_e32 v1, 1, v1
	v_lshrrev_b32_e32 v21, 5, v0
	v_lshlrev_b32_e32 v0, 3, v0
	v_add_co_u32_e32 v30, vcc, s3, v28
	v_bitop3_b32 v1, v1, v21, 7 bitop3:0x78
	v_and_b32_e32 v0, 8, v0
	v_addc_co_u32_e32 v31, vcc, 0, v29, vcc
	v_lshl_or_b32 v0, v1, 4, v0
	v_add_co_u32_e32 v36, vcc, s4, v28
	v_lshl_or_b32 v0, v20, 7, v0
	global_load_dwordx4 v[20:23], v[28:29], off sc0 sc1 nt
	global_load_dwordx4 v[24:27], v[30:31], off sc0 sc1 nt
	v_addc_co_u32_e32 v37, vcc, 0, v29, vcc
	s_add_i32 s0, s2, 0x80
	v_add_co_u32_e32 v38, vcc, s5, v28
	s_and_b32 s0, s0, 0x3c0
	s_nop 0
	v_addc_co_u32_e32 v39, vcc, 0, v29, vcc
	global_load_dwordx4 v[28:31], v[36:37], off sc0 sc1 nt
	global_load_dwordx4 v[32:35], v[38:39], off sc0 sc1 nt
	s_lshl_b32 s0, s0, 2
	v_lshl_add_u64 v[44:45], v[2:3], 0, s[0:1]
	v_add_co_u32_e32 v46, vcc, s3, v44
	s_add_i32 s0, s2, 0xc0
	s_nop 0
	v_addc_co_u32_e32 v47, vcc, 0, v45, vcc
	v_add_co_u32_e32 v52, vcc, s4, v44
	global_load_dwordx4 v[36:39], v[44:45], off sc0 sc1 nt
	global_load_dwordx4 v[40:43], v[46:47], off sc0 sc1 nt
	v_addc_co_u32_e32 v53, vcc, 0, v45, vcc
	v_add_co_u32_e32 v54, vcc, s5, v44
	s_and_b32 s0, s0, 0x3c0
	s_nop 0
	v_addc_co_u32_e32 v55, vcc, 0, v45, vcc
	global_load_dwordx4 v[44:47], v[52:53], off sc0 sc1 nt
	global_load_dwordx4 v[48:51], v[54:55], off sc0 sc1 nt
	s_lshl_b32 s0, s0, 2
	v_lshl_add_u64 v[60:61], v[2:3], 0, s[0:1]
	v_add_co_u32_e32 v62, vcc, s3, v60
	s_add_i32 s0, s2, 0x100
	s_nop 0
	v_addc_co_u32_e32 v63, vcc, 0, v61, vcc
	v_add_co_u32_e32 v68, vcc, s4, v60
	global_load_dwordx4 v[52:55], v[60:61], off sc0 sc1 nt
	global_load_dwordx4 v[56:59], v[62:63], off sc0 sc1 nt
	v_addc_co_u32_e32 v69, vcc, 0, v61, vcc
	v_add_co_u32_e32 v70, vcc, s5, v60
	s_and_b32 s0, s0, 0x3c0
	s_nop 0
	v_addc_co_u32_e32 v71, vcc, 0, v61, vcc
	global_load_dwordx4 v[60:63], v[68:69], off sc0 sc1 nt
	global_load_dwordx4 v[64:67], v[70:71], off sc0 sc1 nt
	s_lshl_b32 s0, s0, 2
	v_add_u32_e32 v1, 0x10000, v0
	s_waitcnt vmcnt(15)
	v_cvt_pk_f16_f32 v7, v6, v7
	v_cvt_pk_f16_f32 v6, v4, v5
	s_waitcnt vmcnt(14)
	v_cvt_pk_f16_f32 v5, v10, v11
	v_cvt_pk_f16_f32 v4, v8, v9
	ds_write2st64_b64 v0, v[6:7], v[4:5] offset1:4
	s_waitcnt vmcnt(13)
	v_cvt_pk_f16_f32 v4, v12, v13
	v_lshl_add_u64 v[12:13], v[2:3], 0, s[0:1]
	v_cvt_pk_f16_f32 v5, v14, v15
	v_add_co_u32_e32 v14, vcc, s3, v12
	s_add_i32 s0, s2, 0x140
	s_nop 0
	v_addc_co_u32_e32 v15, vcc, 0, v13, vcc
	s_waitcnt vmcnt(12)
	v_cvt_pk_f16_f32 v7, v18, v19
	v_cvt_pk_f16_f32 v6, v16, v17
	ds_write2st64_b64 v0, v[4:5], v[6:7] offset0:8 offset1:12
	v_add_co_u32_e32 v68, vcc, s4, v12
	global_load_dwordx4 v[4:7], v[12:13], off sc0 sc1 nt
	global_load_dwordx4 v[8:11], v[14:15], off sc0 sc1 nt
	v_addc_co_u32_e32 v69, vcc, 0, v13, vcc
	v_add_co_u32_e32 v70, vcc, s5, v12
	s_and_b32 s0, s0, 0x3c0
	s_nop 0
	v_addc_co_u32_e32 v71, vcc, 0, v13, vcc
	global_load_dwordx4 v[12:15], v[68:69], off sc0 sc1 nt
	global_load_dwordx4 v[16:19], v[70:71], off sc0 sc1 nt
	s_waitcnt vmcnt(15)
	v_cvt_pk_f16_f32 v23, v22, v23
	v_cvt_pk_f16_f32 v22, v20, v21
	s_waitcnt vmcnt(14)
	v_cvt_pk_f16_f32 v21, v26, v27
	v_cvt_pk_f16_f32 v20, v24, v25
	s_lshl_b32 s0, s0, 2
	s_waitcnt lgkmcnt(0)
	s_barrier
	ds_write2st64_b64 v0, v[22:23], v[20:21] offset0:16 offset1:20
	s_waitcnt vmcnt(13)
	v_cvt_pk_f16_f32 v20, v28, v29
	v_lshl_add_u64 v[28:29], v[2:3], 0, s[0:1]
	v_cvt_pk_f16_f32 v21, v30, v31
	v_add_co_u32_e32 v30, vcc, s3, v28
	s_waitcnt vmcnt(12)
	v_cvt_pk_f16_f32 v23, v34, v35
	v_cvt_pk_f16_f32 v22, v32, v33
	v_addc_co_u32_e32 v31, vcc, 0, v29, vcc
	ds_write2st64_b64 v0, v[20:21], v[22:23] offset0:24 offset1:28
	v_add_co_u32_e32 v68, vcc, s4, v28
	global_load_dwordx4 v[20:23], v[28:29], off sc0 sc1 nt
	global_load_dwordx4 v[24:27], v[30:31], off sc0 sc1 nt
	v_addc_co_u32_e32 v69, vcc, 0, v29, vcc
	s_add_i32 s0, s2, 0x180
	v_add_co_u32_e32 v70, vcc, s5, v28
	s_and_b32 s0, s0, 0x3c0
	s_nop 0
	v_addc_co_u32_e32 v71, vcc, 0, v29, vcc
	global_load_dwordx4 v[28:31], v[68:69], off sc0 sc1 nt
	global_load_dwordx4 v[32:35], v[70:71], off sc0 sc1 nt
	s_waitcnt vmcnt(15)
	v_cvt_pk_f16_f32 v39, v38, v39
	v_cvt_pk_f16_f32 v38, v36, v37
	s_waitcnt vmcnt(14)
	v_cvt_pk_f16_f32 v37, v42, v43
	v_cvt_pk_f16_f32 v36, v40, v41
	s_lshl_b32 s0, s0, 2
	s_waitcnt lgkmcnt(0)
	s_barrier
	ds_write2st64_b64 v0, v[38:39], v[36:37] offset0:32 offset1:36
	s_waitcnt vmcnt(13)
	v_cvt_pk_f16_f32 v36, v44, v45
	v_lshl_add_u64 v[44:45], v[2:3], 0, s[0:1]
	v_cvt_pk_f16_f32 v37, v46, v47
	v_add_co_u32_e32 v46, vcc, s3, v44
	s_waitcnt vmcnt(12)
	v_cvt_pk_f16_f32 v39, v50, v51
	v_cvt_pk_f16_f32 v38, v48, v49
	v_addc_co_u32_e32 v47, vcc, 0, v45, vcc
	ds_write2st64_b64 v0, v[36:37], v[38:39] offset0:40 offset1:44
	v_add_co_u32_e32 v68, vcc, s4, v44
	global_load_dwordx4 v[36:39], v[44:45], off sc0 sc1 nt
	global_load_dwordx4 v[40:43], v[46:47], off sc0 sc1 nt
	v_addc_co_u32_e32 v69, vcc, 0, v45, vcc
	v_add_co_u32_e32 v70, vcc, s5, v44
	s_add_i32 s0, s2, 0x1c0
	s_nop 0
	v_addc_co_u32_e32 v71, vcc, 0, v45, vcc
	global_load_dwordx4 v[44:47], v[68:69], off sc0 sc1 nt
	global_load_dwordx4 v[48:51], v[70:71], off sc0 sc1 nt
	s_and_b32 s0, s0, 0x3c0
	s_waitcnt vmcnt(15)
	v_cvt_pk_f16_f32 v55, v54, v55
	v_cvt_pk_f16_f32 v54, v52, v53
	s_waitcnt vmcnt(14)
	v_cvt_pk_f16_f32 v53, v58, v59
	v_cvt_pk_f16_f32 v52, v56, v57
	s_lshl_b32 s0, s0, 2
	s_waitcnt lgkmcnt(0)
	s_barrier
	ds_write2st64_b64 v0, v[54:55], v[52:53] offset0:48 offset1:52
	s_waitcnt vmcnt(13)
	v_cvt_pk_f16_f32 v52, v60, v61
	v_lshl_add_u64 v[60:61], v[2:3], 0, s[0:1]
	v_cvt_pk_f16_f32 v53, v62, v63
	v_add_co_u32_e32 v62, vcc, s3, v60
	s_waitcnt vmcnt(12)
	v_cvt_pk_f16_f32 v55, v66, v67
	v_addc_co_u32_e32 v63, vcc, 0, v61, vcc
	v_cvt_pk_f16_f32 v54, v64, v65
	v_add_co_u32_e32 v68, vcc, s4, v60
	ds_write2st64_b64 v0, v[52:53], v[54:55] offset0:56 offset1:60
	s_nop 0
	v_addc_co_u32_e32 v69, vcc, 0, v61, vcc
	global_load_dwordx4 v[52:55], v[60:61], off sc0 sc1 nt
	global_load_dwordx4 v[56:59], v[62:63], off sc0 sc1 nt
	v_add_co_u32_e32 v70, vcc, s5, v60
	s_xor_b32 s0, s6, 0x200
	s_nop 0
	v_addc_co_u32_e32 v71, vcc, 0, v61, vcc
	global_load_dwordx4 v[60:63], v[68:69], off sc0 sc1 nt
	global_load_dwordx4 v[64:67], v[70:71], off sc0 sc1 nt
	s_waitcnt vmcnt(15)
	v_cvt_pk_f16_f32 v7, v6, v7
	v_cvt_pk_f16_f32 v6, v4, v5
	s_waitcnt vmcnt(14)
	v_cvt_pk_f16_f32 v5, v10, v11
	v_cvt_pk_f16_f32 v4, v8, v9
	s_lshl_b32 s0, s0, 2
	s_waitcnt lgkmcnt(0)
	s_barrier
	ds_write2st64_b64 v0, v[6:7], v[4:5] offset0:64 offset1:68
	s_waitcnt vmcnt(13)
	v_cvt_pk_f16_f32 v4, v12, v13
	v_lshl_add_u64 v[12:13], v[2:3], 0, s[0:1]
	v_cvt_pk_f16_f32 v5, v14, v15
	v_add_co_u32_e32 v14, vcc, s3, v12
	s_waitcnt vmcnt(12)
	v_cvt_pk_f16_f32 v7, v18, v19
	v_cvt_pk_f16_f32 v6, v16, v17
	v_addc_co_u32_e32 v15, vcc, 0, v13, vcc
	ds_write2st64_b64 v0, v[4:5], v[6:7] offset0:72 offset1:76
	v_add_co_u32_e32 v68, vcc, s4, v12
	global_load_dwordx4 v[4:7], v[12:13], off sc0 sc1 nt
	global_load_dwordx4 v[8:11], v[14:15], off sc0 sc1 nt
	v_addc_co_u32_e32 v69, vcc, 0, v13, vcc
	s_add_i32 s0, s2, 0x240
	v_add_co_u32_e32 v70, vcc, s5, v12
	s_and_b32 s0, s0, 0x3c0
	s_nop 0
	v_addc_co_u32_e32 v71, vcc, 0, v13, vcc
	global_load_dwordx4 v[12:15], v[68:69], off sc0 sc1 nt
	global_load_dwordx4 v[16:19], v[70:71], off sc0 sc1 nt
	s_waitcnt vmcnt(15)
	v_cvt_pk_f16_f32 v23, v22, v23
	v_cvt_pk_f16_f32 v22, v20, v21
	s_waitcnt vmcnt(14)
	v_cvt_pk_f16_f32 v21, v26, v27
	v_cvt_pk_f16_f32 v20, v24, v25
	s_lshl_b32 s0, s0, 2
	s_waitcnt lgkmcnt(0)
	s_barrier
	ds_write2st64_b64 v0, v[22:23], v[20:21] offset0:80 offset1:84
	s_waitcnt vmcnt(13)
	v_cvt_pk_f16_f32 v20, v28, v29
	v_lshl_add_u64 v[28:29], v[2:3], 0, s[0:1]
	v_cvt_pk_f16_f32 v21, v30, v31
	v_add_co_u32_e32 v30, vcc, s3, v28
	s_waitcnt vmcnt(12)
	v_cvt_pk_f16_f32 v23, v34, v35
	v_cvt_pk_f16_f32 v22, v32, v33
	v_addc_co_u32_e32 v31, vcc, 0, v29, vcc
	ds_write2st64_b64 v0, v[20:21], v[22:23] offset0:88 offset1:92
	v_add_co_u32_e32 v68, vcc, s4, v28
	global_load_dwordx4 v[20:23], v[28:29], off sc0 sc1 nt
	global_load_dwordx4 v[24:27], v[30:31], off sc0 sc1 nt
	v_addc_co_u32_e32 v69, vcc, 0, v29, vcc
	s_add_i32 s0, s2, 0x280
	v_add_co_u32_e32 v70, vcc, s5, v28
	s_and_b32 s0, s0, 0x3c0
	s_nop 0
	v_addc_co_u32_e32 v71, vcc, 0, v29, vcc
	global_load_dwordx4 v[28:31], v[68:69], off sc0 sc1 nt
	global_load_dwordx4 v[32:35], v[70:71], off sc0 sc1 nt
	s_waitcnt vmcnt(15)
	v_cvt_pk_f16_f32 v39, v38, v39
	v_cvt_pk_f16_f32 v38, v36, v37
	s_waitcnt vmcnt(14)
	v_cvt_pk_f16_f32 v37, v42, v43
	v_cvt_pk_f16_f32 v36, v40, v41
	s_lshl_b32 s0, s0, 2
	s_waitcnt lgkmcnt(0)
	s_barrier
	ds_write2st64_b64 v0, v[38:39], v[36:37] offset0:96 offset1:100
	s_waitcnt vmcnt(13)
	v_cvt_pk_f16_f32 v36, v44, v45
	v_lshl_add_u64 v[44:45], v[2:3], 0, s[0:1]
	v_cvt_pk_f16_f32 v37, v46, v47
	v_add_co_u32_e32 v46, vcc, s3, v44
	s_waitcnt vmcnt(12)
	v_cvt_pk_f16_f32 v39, v50, v51
	v_cvt_pk_f16_f32 v38, v48, v49
	v_addc_co_u32_e32 v47, vcc, 0, v45, vcc
	ds_write2st64_b64 v0, v[36:37], v[38:39] offset0:104 offset1:108
	v_add_co_u32_e32 v68, vcc, s4, v44
	global_load_dwordx4 v[36:39], v[44:45], off sc0 sc1 nt
	global_load_dwordx4 v[40:43], v[46:47], off sc0 sc1 nt
	v_addc_co_u32_e32 v69, vcc, 0, v45, vcc
	v_add_co_u32_e32 v70, vcc, s5, v44
	s_add_i32 s0, s2, 0x2c0
	s_nop 0
	v_addc_co_u32_e32 v71, vcc, 0, v45, vcc
	global_load_dwordx4 v[44:47], v[68:69], off sc0 sc1 nt
	global_load_dwordx4 v[48:51], v[70:71], off sc0 sc1 nt
	s_and_b32 s0, s0, 0x3c0
	s_waitcnt vmcnt(15)
	v_cvt_pk_f16_f32 v55, v54, v55
	v_cvt_pk_f16_f32 v54, v52, v53
	s_waitcnt vmcnt(14)
	v_cvt_pk_f16_f32 v53, v58, v59
	v_cvt_pk_f16_f32 v52, v56, v57
	s_lshl_b32 s0, s0, 2
	s_waitcnt lgkmcnt(0)
	s_barrier
	ds_write2st64_b64 v0, v[54:55], v[52:53] offset0:112 offset1:116
	s_waitcnt vmcnt(13)
	v_cvt_pk_f16_f32 v53, v62, v63
	v_cvt_pk_f16_f32 v52, v60, v61
	s_waitcnt vmcnt(12)
	v_cvt_pk_f16_f32 v55, v66, v67
	v_cvt_pk_f16_f32 v54, v64, v65
	v_lshl_add_u64 v[60:61], v[2:3], 0, s[0:1]
	ds_write2st64_b64 v0, v[52:53], v[54:55] offset0:120 offset1:124
	v_add_co_u32_e32 v62, vcc, s3, v60
	s_add_i32 s0, s2, 0x300
	s_nop 0
	v_addc_co_u32_e32 v63, vcc, 0, v61, vcc
	global_load_dwordx4 v[52:55], v[60:61], off sc0 sc1 nt
	global_load_dwordx4 v[56:59], v[62:63], off sc0 sc1 nt
	v_add_co_u32_e32 v68, vcc, s4, v60
	s_waitcnt vmcnt(13)
	v_cvt_pk_f16_f32 v7, v6, v7
	v_addc_co_u32_e32 v69, vcc, 0, v61, vcc
	v_add_co_u32_e32 v70, vcc, s5, v60
	v_cvt_pk_f16_f32 v6, v4, v5
	s_and_b32 s0, s0, 0x3c0
	v_addc_co_u32_e32 v71, vcc, 0, v61, vcc
	global_load_dwordx4 v[60:63], v[68:69], off sc0 sc1 nt
	global_load_dwordx4 v[64:67], v[70:71], off sc0 sc1 nt
	s_waitcnt lgkmcnt(0)
	s_barrier
	ds_write_b64 v1, v[6:7]
	s_waitcnt vmcnt(14)
	v_cvt_pk_f16_f32 v5, v10, v11
	v_cvt_pk_f16_f32 v4, v8, v9
	v_add_u32_e32 v1, 0x10800, v0
	s_lshl_b32 s0, s0, 2
	ds_write_b64 v1, v[4:5]
	s_waitcnt vmcnt(13)
	v_cvt_pk_f16_f32 v4, v12, v13
	v_lshl_add_u64 v[12:13], v[2:3], 0, s[0:1]
	v_cvt_pk_f16_f32 v5, v14, v15
	v_add_co_u32_e32 v14, vcc, s3, v12
	v_add_u32_e32 v1, 0x11000, v0
	s_nop 0
	v_addc_co_u32_e32 v15, vcc, 0, v13, vcc
	v_add_co_u32_e32 v68, vcc, s4, v12
	ds_write_b64 v1, v[4:5]
	s_waitcnt vmcnt(12)
	v_cvt_pk_f16_f32 v5, v18, v19
	v_cvt_pk_f16_f32 v4, v16, v17
	v_add_u32_e32 v1, 0x11800, v0
	v_addc_co_u32_e32 v69, vcc, 0, v13, vcc
	s_add_i32 s0, s2, 0x340
	ds_write_b64 v1, v[4:5]
	v_add_co_u32_e32 v70, vcc, s5, v12
	s_waitcnt vmcnt(11)
	v_cvt_pk_f16_f32 v23, v22, v23
	v_cvt_pk_f16_f32 v22, v20, v21
	v_add_u32_e32 v1, 0x12000, v0
	s_and_b32 s0, s0, 0x3c0
	global_load_dwordx4 v[4:7], v[12:13], off sc0 sc1 nt
	global_load_dwordx4 v[8:11], v[14:15], off sc0 sc1 nt
	v_addc_co_u32_e32 v71, vcc, 0, v13, vcc
	global_load_dwordx4 v[12:15], v[68:69], off sc0 sc1 nt
	global_load_dwordx4 v[16:19], v[70:71], off sc0 sc1 nt
	s_waitcnt lgkmcnt(0)
	s_barrier
	ds_write_b64 v1, v[22:23]
	s_waitcnt vmcnt(14)
	v_cvt_pk_f16_f32 v21, v26, v27
	v_cvt_pk_f16_f32 v20, v24, v25
	v_add_u32_e32 v1, 0x12800, v0
	s_lshl_b32 s0, s0, 2
	ds_write_b64 v1, v[20:21]
	s_waitcnt vmcnt(13)
	v_cvt_pk_f16_f32 v20, v28, v29
	v_lshl_add_u64 v[28:29], v[2:3], 0, s[0:1]
	v_cvt_pk_f16_f32 v21, v30, v31
	v_add_co_u32_e32 v30, vcc, s3, v28
	v_add_u32_e32 v1, 0x13000, v0
	s_nop 0
	v_addc_co_u32_e32 v31, vcc, 0, v29, vcc
	v_add_co_u32_e32 v68, vcc, s4, v28
	ds_write_b64 v1, v[20:21]
	s_waitcnt vmcnt(12)
	v_cvt_pk_f16_f32 v21, v34, v35
	v_cvt_pk_f16_f32 v20, v32, v33
	v_add_u32_e32 v1, 0x13800, v0
	v_addc_co_u32_e32 v69, vcc, 0, v29, vcc
	s_add_i32 s0, s2, 0x380
	ds_write_b64 v1, v[20:21]
	v_add_co_u32_e32 v70, vcc, s5, v28
	s_waitcnt vmcnt(11)
	v_cvt_pk_f16_f32 v39, v38, v39
	v_cvt_pk_f16_f32 v38, v36, v37
	v_add_u32_e32 v1, 0x14000, v0
	s_and_b32 s0, s0, 0x3c0
	global_load_dwordx4 v[20:23], v[28:29], off sc0 sc1 nt
	global_load_dwordx4 v[24:27], v[30:31], off sc0 sc1 nt
	v_addc_co_u32_e32 v71, vcc, 0, v29, vcc
	global_load_dwordx4 v[28:31], v[68:69], off sc0 sc1 nt
	global_load_dwordx4 v[32:35], v[70:71], off sc0 sc1 nt
	s_waitcnt lgkmcnt(0)
	s_barrier
	ds_write_b64 v1, v[38:39]
	s_waitcnt vmcnt(14)
	v_cvt_pk_f16_f32 v37, v42, v43
	v_cvt_pk_f16_f32 v36, v40, v41
	v_add_u32_e32 v1, 0x14800, v0
	s_lshl_b32 s0, s0, 2
	ds_write_b64 v1, v[36:37]
	s_waitcnt vmcnt(13)
	v_cvt_pk_f16_f32 v36, v44, v45
	v_lshl_add_u64 v[44:45], v[2:3], 0, s[0:1]
	v_cvt_pk_f16_f32 v37, v46, v47
	v_add_co_u32_e32 v46, vcc, s3, v44
	s_addk_i32 s2, 0x3c0
	s_nop 0
	v_addc_co_u32_e32 v47, vcc, 0, v45, vcc
	v_add_co_u32_e32 v68, vcc, s4, v44
	v_add_u32_e32 v1, 0x15000, v0
	s_nop 0
	v_addc_co_u32_e32 v69, vcc, 0, v45, vcc
	s_and_b32 s0, s2, 0x3c0
	ds_write_b64 v1, v[36:37]
	s_waitcnt vmcnt(12)
	v_cvt_pk_f16_f32 v37, v50, v51
	v_cvt_pk_f16_f32 v36, v48, v49
	v_add_u32_e32 v1, 0x15800, v0
	v_add_co_u32_e32 v70, vcc, s5, v44
	s_lshl_b32 s0, s0, 2
	ds_write_b64 v1, v[36:37]
	v_addc_co_u32_e32 v71, vcc, 0, v45, vcc
	v_lshl_add_u64 v[2:3], v[2:3], 0, s[0:1]
	global_load_dwordx4 v[36:39], v[44:45], off sc0 sc1 nt
	global_load_dwordx4 v[40:43], v[46:47], off sc0 sc1 nt
	s_waitcnt vmcnt(13)
	v_cvt_pk_f16_f32 v55, v54, v55
	v_cvt_pk_f16_f32 v54, v52, v53
	s_waitcnt vmcnt(12)
	v_cvt_pk_f16_f32 v52, v56, v57
	v_add_co_u32_e32 v56, vcc, s3, v2
	v_add_u32_e32 v1, 0x16000, v0
	s_nop 0
	v_addc_co_u32_e32 v57, vcc, 0, v3, vcc
	global_load_dwordx4 v[44:47], v[68:69], off sc0 sc1 nt
	global_load_dwordx4 v[48:51], v[70:71], off sc0 sc1 nt
	s_waitcnt lgkmcnt(0)
	s_barrier
	ds_write_b64 v1, v[54:55]
	v_cvt_pk_f16_f32 v53, v58, v59
	v_add_u32_e32 v1, 0x16800, v0
	v_add_co_u32_e32 v68, vcc, s4, v2
	ds_write_b64 v1, v[52:53]
	global_load_dwordx4 v[52:55], v[2:3], off sc0 sc1 nt
	v_addc_co_u32_e32 v69, vcc, 0, v3, vcc
	global_load_dwordx4 v[56:59], v[56:57], off sc0 sc1 nt
	v_add_co_u32_e32 v2, vcc, s5, v2
	global_load_dwordx4 v[68:71], v[68:69], off sc0 sc1 nt
	s_nop 0
	v_addc_co_u32_e32 v3, vcc, 0, v3, vcc
	global_load_dwordx4 v[72:75], v[2:3], off sc0 sc1 nt
	s_waitcnt vmcnt(17)
	v_cvt_pk_f16_f32 v63, v62, v63
	v_cvt_pk_f16_f32 v62, v60, v61
	v_add_u32_e32 v1, 0x17000, v0
	ds_write_b64 v1, v[62:63]
	s_waitcnt vmcnt(16)
	v_cvt_pk_f16_f32 v3, v66, v67
	v_cvt_pk_f16_f32 v2, v64, v65
	v_add_u32_e32 v1, 0x17800, v0
	ds_write_b64 v1, v[2:3]
	s_waitcnt vmcnt(15)
	v_cvt_pk_f16_f32 v3, v6, v7
	v_cvt_pk_f16_f32 v2, v4, v5
	v_add_u32_e32 v1, 0x18000, v0
	s_waitcnt lgkmcnt(0)
	s_barrier
	ds_write_b64 v1, v[2:3]
	s_waitcnt vmcnt(14)
	v_cvt_pk_f16_f32 v3, v10, v11
	v_cvt_pk_f16_f32 v2, v8, v9
	v_add_u32_e32 v1, 0x18800, v0
	ds_write_b64 v1, v[2:3]
	s_waitcnt vmcnt(13)
	v_cvt_pk_f16_f32 v3, v14, v15
	v_cvt_pk_f16_f32 v2, v12, v13
	v_add_u32_e32 v1, 0x19000, v0
	ds_write_b64 v1, v[2:3]
	s_waitcnt vmcnt(12)
	v_cvt_pk_f16_f32 v3, v18, v19
	v_cvt_pk_f16_f32 v2, v16, v17
	v_add_u32_e32 v1, 0x19800, v0
	ds_write_b64 v1, v[2:3]
	s_waitcnt vmcnt(11)
	v_cvt_pk_f16_f32 v3, v22, v23
	v_cvt_pk_f16_f32 v2, v20, v21
	v_add_u32_e32 v1, 0x1a000, v0
	s_waitcnt lgkmcnt(0)
	s_barrier
	ds_write_b64 v1, v[2:3]
	s_waitcnt vmcnt(10)
	v_cvt_pk_f16_f32 v3, v26, v27
	v_cvt_pk_f16_f32 v2, v24, v25
	v_add_u32_e32 v1, 0x1a800, v0
	ds_write_b64 v1, v[2:3]
	s_waitcnt vmcnt(9)
	v_cvt_pk_f16_f32 v3, v30, v31
	v_cvt_pk_f16_f32 v2, v28, v29
	v_add_u32_e32 v1, 0x1b000, v0
	ds_write_b64 v1, v[2:3]
	s_waitcnt vmcnt(8)
	v_cvt_pk_f16_f32 v3, v34, v35
	v_cvt_pk_f16_f32 v2, v32, v33
	v_add_u32_e32 v1, 0x1b800, v0
	ds_write_b64 v1, v[2:3]
	v_add_u32_e32 v1, 0x1c000, v0
	s_waitcnt lgkmcnt(0)
	s_barrier
	s_waitcnt vmcnt(7)
	v_cvt_pk_f16_f32 v3, v38, v39
	v_cvt_pk_f16_f32 v2, v36, v37
	ds_write_b64 v1, v[2:3]
	s_waitcnt vmcnt(6)
	v_cvt_pk_f16_f32 v3, v42, v43
	v_cvt_pk_f16_f32 v2, v40, v41
	v_add_u32_e32 v1, 0x1c800, v0
	ds_write_b64 v1, v[2:3]
	v_add_u32_e32 v1, 0x1d000, v0
	s_waitcnt vmcnt(5)
	v_cvt_pk_f16_f32 v3, v46, v47
	v_cvt_pk_f16_f32 v2, v44, v45
	ds_write_b64 v1, v[2:3]
	s_waitcnt vmcnt(4)
	v_cvt_pk_f16_f32 v3, v50, v51
	v_cvt_pk_f16_f32 v2, v48, v49
	v_add_u32_e32 v1, 0x1d800, v0
	ds_write_b64 v1, v[2:3]
	v_add_u32_e32 v1, 0x1e000, v0
	s_waitcnt lgkmcnt(0)
	s_barrier
	s_waitcnt vmcnt(3)
	v_cvt_pk_f16_f32 v3, v54, v55
	v_cvt_pk_f16_f32 v2, v52, v53
	ds_write_b64 v1, v[2:3]
	s_waitcnt vmcnt(2)
	v_cvt_pk_f16_f32 v3, v58, v59
	v_cvt_pk_f16_f32 v2, v56, v57
	v_add_u32_e32 v1, 0x1e800, v0
	ds_write_b64 v1, v[2:3]
	s_waitcnt vmcnt(1)
	v_cvt_pk_f16_f32 v3, v70, v71
	v_cvt_pk_f16_f32 v2, v68, v69
	v_add_u32_e32 v1, 0x1f000, v0
	ds_write_b64 v1, v[2:3]
	s_waitcnt vmcnt(0)
	v_cvt_pk_f16_f32 v3, v74, v75
	v_cvt_pk_f16_f32 v2, v72, v73
	v_add_u32_e32 v0, 0x1f800, v0
	ds_write_b64 v0, v[2:3]
	s_waitcnt lgkmcnt(0)
	s_barrier
	s_endpgm
